# final_phase_deferred_stores_behind_next_gather
# speedup vs baseline: 1.0108x; 1.0018x over previous
.Lfin_pf_first:
	s_mov_b32 s28, 0
	s_mov_b32 s52, 0
	s_mov_b32 s53, 0

.Lfin_pf_next:
	s_mov_b32 s28, 1
.Lfin_round:
	s_mov_b32 s36, 0
	s_cmp_eq_u32 s30, 0
	s_cbranch_scc1 .Lfin_iss_A_done
	s_ff1_i32_b32 s14, s30
	s_bitset0_b32 s30, s14
	v_readlane_b32 s15, v18, s14
	s_lshl_b32 s15, s15, 11
	s_add_u32 s16, s8, s15
	s_addc_u32 s17, s9, 0
	global_load_dwordx2 v[128:129], v105, s[16:17]
	global_load_dwordx2 v[130:131], v105, s[16:17] offset:512
	global_load_dwordx2 v[132:133], v105, s[16:17] offset:1024
	global_load_dwordx2 v[134:135], v105, s[16:17] offset:1536
	s_bitset1_b32 s36, 0
	s_cmp_eq_u32 s30, 0
	s_cbranch_scc1 .Lfin_iss_A_done
	s_ff1_i32_b32 s14, s30
	s_bitset0_b32 s30, s14
	v_readlane_b32 s15, v18, s14
	s_lshl_b32 s15, s15, 11
	s_add_u32 s16, s8, s15
	s_addc_u32 s17, s9, 0
	global_load_dwordx2 v[136:137], v105, s[16:17]
	global_load_dwordx2 v[138:139], v105, s[16:17] offset:512
	global_load_dwordx2 v[140:141], v105, s[16:17] offset:1024
	global_load_dwordx2 v[142:143], v105, s[16:17] offset:1536
	s_bitset1_b32 s36, 1
	s_cmp_eq_u32 s30, 0
	s_cbranch_scc1 .Lfin_iss_A_done
	s_ff1_i32_b32 s14, s30
	s_bitset0_b32 s30, s14
	v_readlane_b32 s15, v18, s14
	s_lshl_b32 s15, s15, 11
	s_add_u32 s16, s8, s15
	s_addc_u32 s17, s9, 0
	global_load_dwordx2 v[144:145], v105, s[16:17]
	global_load_dwordx2 v[146:147], v105, s[16:17] offset:512
	global_load_dwordx2 v[148:149], v105, s[16:17] offset:1024
	global_load_dwordx2 v[150:151], v105, s[16:17] offset:1536
	s_bitset1_b32 s36, 2
	s_cmp_eq_u32 s30, 0
	s_cbranch_scc1 .Lfin_iss_A_done
	s_ff1_i32_b32 s14, s30
	s_bitset0_b32 s30, s14
	v_readlane_b32 s15, v18, s14
	s_lshl_b32 s15, s15, 11
	s_add_u32 s16, s8, s15
	s_addc_u32 s17, s9, 0
	global_load_dwordx2 v[152:153], v105, s[16:17]
	global_load_dwordx2 v[154:155], v105, s[16:17] offset:512
	global_load_dwordx2 v[156:157], v105, s[16:17] offset:1024
	global_load_dwordx2 v[158:159], v105, s[16:17] offset:1536
	s_bitset1_b32 s36, 3

.Lfin_iss_B_done:
	s_cmp_eq_u32 s52, 0
	s_cbranch_scc1 .Lfin_ds_none
	global_store_dwordx4 v107, v[192:195], s[48:49]
	global_store_dwordx4 v107, v[196:199], s[48:49] offset:1024
	global_store_dwordx4 v107, v[200:203], s[48:49] offset:2048
	global_store_dwordx4 v107, v[204:207], s[48:49] offset:3072
	s_mov_b32 s52, 0
	s_cmp_eq_u32 s53, 0
	s_cbranch_scc1 .Lfin_ds_one
	global_store_dwordx4 v107, v[208:211], s[50:51]
	global_store_dwordx4 v107, v[212:215], s[50:51] offset:1024
	global_store_dwordx4 v107, v[216:219], s[50:51] offset:2048
	global_store_dwordx4 v107, v[220:223], s[50:51] offset:3072
	s_mov_b32 s53, 0
	s_waitcnt vmcnt(8)
	s_branch .Lfin_ds_done
.Lfin_ds_one:
	s_waitcnt vmcnt(4)
	s_branch .Lfin_ds_done

.Lfin_ds_done:
	s_bitcmp1_b32 s36, 0
	s_cbranch_scc0 .Lfin_add_skip_0
	v_lshlrev_b32_e32 v64, 16, v128
	v_and_b32_e32 v65, 0xffff0000, v128
	v_pk_add_f32 v[32:33], v[32:33], v[64:65]
	v_lshlrev_b32_e32 v66, 16, v129
	v_and_b32_e32 v67, 0xffff0000, v129
	v_pk_add_f32 v[34:35], v[34:35], v[66:67]
	v_lshlrev_b32_e32 v68, 16, v130
	v_and_b32_e32 v69, 0xffff0000, v130
	v_pk_add_f32 v[36:37], v[36:37], v[68:69]
	v_lshlrev_b32_e32 v70, 16, v131
	v_and_b32_e32 v71, 0xffff0000, v131
	v_pk_add_f32 v[38:39], v[38:39], v[70:71]
	v_lshlrev_b32_e32 v72, 16, v132
	v_and_b32_e32 v73, 0xffff0000, v132
	v_pk_add_f32 v[40:41], v[40:41], v[72:73]
	v_lshlrev_b32_e32 v74, 16, v133
	v_and_b32_e32 v75, 0xffff0000, v133
	v_pk_add_f32 v[42:43], v[42:43], v[74:75]
	v_lshlrev_b32_e32 v76, 16, v134
	v_and_b32_e32 v77, 0xffff0000, v134
	v_pk_add_f32 v[44:45], v[44:45], v[76:77]
	v_lshlrev_b32_e32 v78, 16, v135
	v_and_b32_e32 v79, 0xffff0000, v135
	v_pk_add_f32 v[46:47], v[46:47], v[78:79]

.Lfin_rounds_done:
	v_mul_f32_e32 v94, v33, v33
	v_mul_f32_e32 v95, v35, v35
	v_mul_f32_e32 v96, v37, v37
	v_mul_f32_e32 v97, v39, v39
	v_mul_f32_e32 v98, v41, v41
	v_mul_f32_e32 v99, v43, v43
	v_mul_f32_e32 v100, v45, v45
	v_mul_f32_e32 v101, v47, v47
	v_fmac_f32_e32 v94, v32, v32
	v_fmac_f32_e32 v95, v34, v34
	v_fmac_f32_e32 v96, v36, v36
	v_fmac_f32_e32 v97, v38, v38
	v_fmac_f32_e32 v98, v40, v40
	v_fmac_f32_e32 v99, v42, v42
	v_fmac_f32_e32 v100, v44, v44
	v_fmac_f32_e32 v101, v46, v46
	v_add_f32_e32 v94, v94, v95
	v_add_f32_e32 v96, v96, v97
	v_add_f32_e32 v98, v98, v99
	v_add_f32_e32 v100, v100, v101
	v_add_f32_e32 v84, v96, v94
	v_add_f32_e32 v84, v98, v84
	v_add_f32_e32 v84, v100, v84
	s_lshl_b32 s10, s2, 12
	s_add_u32 s10, s24, s10
	s_addc_u32 s11, s25, 0
	s_nop 1
	v_add_f32_dpp v84, v84, v84 quad_perm:[1,0,3,2] row_mask:0xf bank_mask:0xf bound_ctrl:1
	s_nop 1
	v_add_f32_dpp v84, v84, v84 quad_perm:[2,3,0,1] row_mask:0xf bank_mask:0xf bound_ctrl:1
	s_nop 1
	v_add_f32_dpp v84, v84, v84 row_half_mirror row_mask:0xf bank_mask:0xf bound_ctrl:1
	s_nop 1
	v_add_f32_dpp v84, v84, v84 row_mirror row_mask:0xf bank_mask:0xf bound_ctrl:1
	v_mov_b32_e32 v85, v84
	s_nop 1
	v_permlane16_swap_b32_e32 v84, v85
	v_add_f32_e32 v84, v84, v85
	v_mov_b32_e32 v85, v84
	s_nop 1
	v_permlane32_swap_b32_e32 v84, v85
	v_add_f32_e32 v84, v84, v85
	v_fmamk_f32 v84, v84, 0x3a800000, v108
	v_mul_f32_e32 v85, 0x4f800000, v84
	v_cmp_gt_f32_e32 vcc, s35, v84
	s_nop 1
	v_cndmask_b32_e32 v84, v84, v85, vcc
	v_sqrt_f32_e32 v85, v84
	s_nop 0
	v_add_u32_e32 v86, -1, v85
	v_add_u32_e32 v91, 1, v85
	v_fma_f32 v89, -v86, v85, v84
	v_fma_f32 v90, -v91, v85, v84
	v_cmp_ge_f32_e64 s[12:13], 0, v89
	s_nop 1
	v_cndmask_b32_e64 v85, v85, v86, s[12:13]
	v_cmp_lt_f32_e64 s[12:13], 0, v90
	s_nop 1
	v_cndmask_b32_e64 v85, v85, v91, s[12:13]
	v_mul_f32_e32 v86, 0x37800000, v85
	v_cndmask_b32_e32 v85, v85, v86, vcc
	v_cmp_class_f32_e32 vcc, v84, v109
	s_nop 1
	v_cndmask_b32_e32 v84, v85, v84, vcc
	v_div_scale_f32 v88, s[12:13], v84, v84, 1.0
	v_rcp_f32_e32 v89, v88
	v_div_scale_f32 v90, vcc, 1.0, v84, 1.0
	s_nop 0
	v_fma_f32 v91, -v88, v89, 1.0
	v_fmac_f32_e32 v89, v91, v89
	v_mul_f32_e32 v91, v90, v89
	v_fma_f32 v92, -v88, v91, v90
	v_fmac_f32_e32 v91, v92, v89
	v_fma_f32 v88, -v88, v91, v90
	v_div_fmas_f32 v88, v88, v89, v91
	v_div_fixup_f32 v88, v88, v84, 1.0
	v_pk_mul_f32 v[32:33], v[88:89], v[32:33] op_sel_hi:[0,1]
	v_pk_mul_f32 v[34:35], v[88:89], v[34:35] op_sel_hi:[0,1]
	v_pk_mul_f32 v[36:37], v[88:89], v[36:37] op_sel_hi:[0,1]
	v_pk_mul_f32 v[38:39], v[88:89], v[38:39] op_sel_hi:[0,1]
	v_pk_mul_f32 v[40:41], v[88:89], v[40:41] op_sel_hi:[0,1]
	v_pk_mul_f32 v[42:43], v[88:89], v[42:43] op_sel_hi:[0,1]
	v_pk_mul_f32 v[44:45], v[88:89], v[44:45] op_sel_hi:[0,1]
	v_pk_mul_f32 v[46:47], v[88:89], v[46:47] op_sel_hi:[0,1]
	v_pk_mul_f32 v[192:193], v[112:113], v[32:33]
	v_pk_mul_f32 v[194:195], v[114:115], v[34:35]
	v_pk_mul_f32 v[196:197], v[116:117], v[36:37]
	v_pk_mul_f32 v[198:199], v[118:119], v[38:39]
	v_pk_mul_f32 v[200:201], v[120:121], v[40:41]
	v_pk_mul_f32 v[202:203], v[122:123], v[42:43]
	v_pk_mul_f32 v[204:205], v[124:125], v[44:45]
	v_pk_mul_f32 v[206:207], v[126:127], v[46:47]
	s_mov_b32 s48, s10
	s_mov_b32 s49, s11
	s_mov_b32 s52, 1
	s_cmp_eq_u32 s29, 0
	s_cbranch_scc1 .Lfin_skipB
	v_mul_f32_e32 v94, v49, v49
	v_mul_f32_e32 v95, v51, v51
	v_mul_f32_e32 v96, v53, v53
	v_mul_f32_e32 v97, v55, v55
	v_mul_f32_e32 v98, v57, v57
	v_mul_f32_e32 v99, v59, v59
	v_mul_f32_e32 v100, v61, v61
	v_mul_f32_e32 v101, v63, v63
	v_fmac_f32_e32 v94, v48, v48
	v_fmac_f32_e32 v95, v50, v50
	v_fmac_f32_e32 v96, v52, v52
	v_fmac_f32_e32 v97, v54, v54
	v_fmac_f32_e32 v98, v56, v56
	v_fmac_f32_e32 v99, v58, v58
	v_fmac_f32_e32 v100, v60, v60
	v_fmac_f32_e32 v101, v62, v62
	v_add_f32_e32 v94, v94, v95
	v_add_f32_e32 v96, v96, v97
	v_add_f32_e32 v98, v98, v99
	v_add_f32_e32 v100, v100, v101
	v_add_f32_e32 v84, v96, v94
	v_add_f32_e32 v84, v98, v84
	v_add_f32_e32 v84, v100, v84
	s_lshl_b32 s10, s3, 12
	s_add_u32 s10, s24, s10
	s_addc_u32 s11, s25, 0
	s_nop 1
	v_add_f32_dpp v84, v84, v84 quad_perm:[1,0,3,2] row_mask:0xf bank_mask:0xf bound_ctrl:1
	s_nop 1
	v_add_f32_dpp v84, v84, v84 quad_perm:[2,3,0,1] row_mask:0xf bank_mask:0xf bound_ctrl:1
	s_nop 1
	v_add_f32_dpp v84, v84, v84 row_half_mirror row_mask:0xf bank_mask:0xf bound_ctrl:1
	s_nop 1
	v_add_f32_dpp v84, v84, v84 row_mirror row_mask:0xf bank_mask:0xf bound_ctrl:1
	v_mov_b32_e32 v85, v84
	s_nop 1
	v_permlane16_swap_b32_e32 v84, v85
	v_add_f32_e32 v84, v84, v85
	v_mov_b32_e32 v85, v84
	s_nop 1
	v_permlane32_swap_b32_e32 v84, v85
	v_add_f32_e32 v84, v84, v85
	v_fmamk_f32 v84, v84, 0x3a800000, v108
	v_mul_f32_e32 v85, 0x4f800000, v84
	v_cmp_gt_f32_e32 vcc, s35, v84
	s_nop 1
	v_cndmask_b32_e32 v84, v84, v85, vcc
	v_sqrt_f32_e32 v85, v84
	s_nop 0
	v_add_u32_e32 v86, -1, v85
	v_add_u32_e32 v91, 1, v85
	v_fma_f32 v89, -v86, v85, v84
	v_fma_f32 v90, -v91, v85, v84
	v_cmp_ge_f32_e64 s[12:13], 0, v89
	s_nop 1
	v_cndmask_b32_e64 v85, v85, v86, s[12:13]
	v_cmp_lt_f32_e64 s[12:13], 0, v90
	s_nop 1
	v_cndmask_b32_e64 v85, v85, v91, s[12:13]
	v_mul_f32_e32 v86, 0x37800000, v85
	v_cndmask_b32_e32 v85, v85, v86, vcc
	v_cmp_class_f32_e32 vcc, v84, v109
	s_nop 1
	v_cndmask_b32_e32 v84, v85, v84, vcc
	v_div_scale_f32 v88, s[12:13], v84, v84, 1.0
	v_rcp_f32_e32 v89, v88
	v_div_scale_f32 v90, vcc, 1.0, v84, 1.0
	s_nop 0
	v_fma_f32 v91, -v88, v89, 1.0
	v_fmac_f32_e32 v89, v91, v89
	v_mul_f32_e32 v91, v90, v89
	v_fma_f32 v92, -v88, v91, v90
	v_fmac_f32_e32 v91, v92, v89
	v_fma_f32 v88, -v88, v91, v90
	v_div_fmas_f32 v88, v88, v89, v91
	v_div_fixup_f32 v88, v88, v84, 1.0
	v_pk_mul_f32 v[48:49], v[88:89], v[48:49] op_sel_hi:[0,1]
	v_pk_mul_f32 v[50:51], v[88:89], v[50:51] op_sel_hi:[0,1]
	v_pk_mul_f32 v[52:53], v[88:89], v[52:53] op_sel_hi:[0,1]
	v_pk_mul_f32 v[54:55], v[88:89], v[54:55] op_sel_hi:[0,1]
	v_pk_mul_f32 v[56:57], v[88:89], v[56:57] op_sel_hi:[0,1]
	v_pk_mul_f32 v[58:59], v[88:89], v[58:59] op_sel_hi:[0,1]
	v_pk_mul_f32 v[60:61], v[88:89], v[60:61] op_sel_hi:[0,1]
	v_pk_mul_f32 v[62:63], v[88:89], v[62:63] op_sel_hi:[0,1]
	v_pk_mul_f32 v[208:209], v[112:113], v[48:49]
	v_pk_mul_f32 v[210:211], v[114:115], v[50:51]
	v_pk_mul_f32 v[212:213], v[116:117], v[52:53]
	v_pk_mul_f32 v[214:215], v[118:119], v[54:55]
	v_pk_mul_f32 v[216:217], v[120:121], v[56:57]
	v_pk_mul_f32 v[218:219], v[122:123], v[58:59]
	v_pk_mul_f32 v[220:221], v[124:125], v[60:61]
	v_pk_mul_f32 v[222:223], v[126:127], v[62:63]
	s_mov_b32 s50, s10
	s_mov_b32 s51, s11
	s_mov_b32 s53, 1
.Lfin_skipB:
	s_add_i32 s2, s2, s21
	s_cmp_lt_i32 s2, 0x8000
	s_cbranch_scc1 .Lfin_loop
	s_cmp_eq_u32 s52, 0
	s_cbranch_scc1 .LBB0_1150
	global_store_dwordx4 v107, v[192:195], s[48:49]
	global_store_dwordx4 v107, v[196:199], s[48:49] offset:1024
	global_store_dwordx4 v107, v[200:203], s[48:49] offset:2048
	global_store_dwordx4 v107, v[204:207], s[48:49] offset:3072
	s_cmp_eq_u32 s53, 0
	s_cbranch_scc1 .LBB0_1150
	global_store_dwordx4 v107, v[208:211], s[50:51]
	global_store_dwordx4 v107, v[212:215], s[50:51] offset:1024
	global_store_dwordx4 v107, v[216:219], s[50:51] offset:2048
	global_store_dwordx4 v107, v[220:223], s[50:51] offset:3072
